# speedup vs baseline: 1.0000x; 1.0000x over previous
	.amdhsa_kernel _Z9k_coarse2PKtS0_PKdS2_Pf
		.amdhsa_group_segment_fixed_size 256
		.amdhsa_private_segment_fixed_size 0
		.amdhsa_kernarg_size 40
		.amdhsa_user_sgpr_count 2
		.amdhsa_user_sgpr_dispatch_ptr 0
		.amdhsa_user_sgpr_queue_ptr 0
		.amdhsa_user_sgpr_kernarg_segment_ptr 1
		.amdhsa_user_sgpr_dispatch_id 0
		.amdhsa_user_sgpr_kernarg_preload_length 0
		.amdhsa_user_sgpr_kernarg_preload_offset 0
		.amdhsa_user_sgpr_private_segment_size 0
		.amdhsa_uses_dynamic_stack 0
		.amdhsa_enable_private_segment 0
		.amdhsa_system_sgpr_workgroup_id_x 1
		.amdhsa_system_sgpr_workgroup_id_y 0
		.amdhsa_system_sgpr_workgroup_id_z 0
		.amdhsa_system_sgpr_workgroup_info 0
		.amdhsa_system_vgpr_workitem_id 0
		.amdhsa_next_free_vgpr 224
		.amdhsa_next_free_sgpr 40
		.amdhsa_accum_offset 208
		.amdhsa_reserve_vcc 1
		.amdhsa_float_round_mode_32 0
		.amdhsa_float_round_mode_16_64 0
		.amdhsa_float_denorm_mode_32 3
		.amdhsa_float_denorm_mode_16_64 3
		.amdhsa_dx10_clamp 1
		.amdhsa_ieee_mode 1
		.amdhsa_fp16_overflow 0
		.amdhsa_tg_split 0
		.amdhsa_exception_fp_ieee_invalid_op 0
		.amdhsa_exception_fp_denorm_src 0
		.amdhsa_exception_fp_ieee_div_zero 0
		.amdhsa_exception_fp_ieee_overflow 0
		.amdhsa_exception_fp_ieee_underflow 0
		.amdhsa_exception_fp_ieee_inexact 0
		.amdhsa_exception_int_div_zero 0
	.end_amdhsa_kernel

.LBB3_32:
	s_ashr_i32 s12, s2, 3
	s_lshl_b32 s6, s12, 1
	s_ashr_i32 s7, s6, 31
	s_lshl_b64 s[6:7], s[6:7], 2
	s_waitcnt lgkmcnt(0)
	s_add_u32 s8, s14, s6
	s_addc_u32 s9, s15, s7
	s_mov_b64 s[4:5], s[30:31]
	s_load_dwordx2 s[6:7], s[8:9], 0x0
	v_cmp_gt_u32_e32 vcc, 64, v0
	v_lshlrev_b32_e32 v1, 2, v0
	s_and_saveexec_b64 s[8:9], vcc
	v_lshl_or_b32 v2, s12, 6, v0
	v_ashrrev_i32_e32 v3, 31, v2
	v_lshlrev_b64 v[2:3], 2, v[2:3]
	v_lshl_add_u64 v[4:5], s[16:17], 0, v[2:3]
	v_lshl_add_u64 v[2:3], s[18:19], 0, v[2:3]
	global_load_dword v40, v[4:5], off
	global_load_dword v41, v[2:3], off
	v_add_u32_e32 v42, 0x50, v1
	s_or_b64 exec, exec, s[8:9]
	s_ashr_i32 s8, s2, 9
	s_ashr_i32 s9, s8, 31
	s_waitcnt lgkmcnt(0)
	s_lshl_b32 s3, s6, 6
	s_lshl_b64 s[10:11], s[8:9], 12
	s_ashr_i32 s6, s3, 31
	s_add_u32 s3, s10, s3
	s_addc_u32 s9, s11, s6
	s_ashr_i32 s10, s7, 31
	s_add_u32 s6, s3, s7
	s_addc_u32 s7, s9, s10
	s_lshl_b64 s[6:7], s[6:7], 9
	s_add_u32 s3, s4, s6
	s_addc_u32 s5, s5, s7
	s_lshl_b32 s4, s2, 4
	s_and_b32 s9, s4, 0x70
	s_lshl_b32 s4, s9, 2
	s_add_u32 s4, s3, s4
	v_and_b32_e32 v1, 12, v1
	s_movk_i32 s3, 0x384
	s_addc_u32 s5, s5, 0
	v_mov_b32_e32 v33, 49
	s_movk_i32 s3, 0x50
	v_mov_b32_e32 v28, v0
	v_mul_u32_u24_e32 v29, 0x445, v28
	v_lshrrev_b32_e32 v32, 2, v28
	v_lshlrev_b32_e32 v34, 4, v28
	v_mul_lo_u16_sdwa v29, v29, v33 dst_sel:DWORD dst_unused:UNUSED_PAD src0_sel:WORD_1 src1_sel:DWORD
	v_and_b32_e32 v34, 48, v34
	v_add_lshl_u32 v30, v32, v29, 9
	v_add_u32_e32 v30, v30, v34
	global_load_dwordx4 v[8:11], v30, s[4:5]
	v_mad_u32_u24 v24, v32, s3, v34
	v_or_b32_e32 v28, 0x100, v0
	v_mul_u32_u24_e32 v29, 0x445, v28
	v_lshrrev_b32_e32 v32, 2, v28
	v_lshlrev_b32_e32 v34, 4, v28
	v_mul_lo_u16_sdwa v29, v29, v33 dst_sel:DWORD dst_unused:UNUSED_PAD src0_sel:WORD_1 src1_sel:DWORD
	v_and_b32_e32 v34, 48, v34
	v_add_lshl_u32 v31, v32, v29, 9
	v_add_u32_e32 v31, v31, v34
	global_load_dwordx4 v[12:15], v31, s[4:5]
	v_mad_u32_u24 v25, v32, s3, v34
	v_or_b32_e32 v28, 0x200, v0
	v_mul_u32_u24_e32 v29, 0x445, v28
	v_lshrrev_b32_e32 v32, 2, v28
	v_lshlrev_b32_e32 v34, 4, v28
	v_mul_lo_u16_sdwa v29, v29, v33 dst_sel:DWORD dst_unused:UNUSED_PAD src0_sel:WORD_1 src1_sel:DWORD
	v_and_b32_e32 v34, 48, v34
	v_add_lshl_u32 v36, v32, v29, 9
	v_add_u32_e32 v36, v36, v34
	global_load_dwordx4 v[16:19], v36, s[4:5]
	v_mad_u32_u24 v26, v32, s3, v34
	v_or_b32_e32 v28, 0x300, v0
	v_min_u32_e32 v28, 0x383, v28
	v_mul_u32_u24_e32 v29, 0x445, v28
	v_lshrrev_b32_e32 v32, 2, v28
	v_lshlrev_b32_e32 v34, 4, v28
	v_mul_lo_u16_sdwa v29, v29, v33 dst_sel:DWORD dst_unused:UNUSED_PAD src0_sel:WORD_1 src1_sel:DWORD
	v_and_b32_e32 v34, 48, v34
	v_add_lshl_u32 v37, v32, v29, 9
	v_add_u32_e32 v37, v37, v34
	global_load_dwordx4 v[20:23], v37, s[4:5]
	v_mad_u32_u24 v27, v32, s3, v34
	v_cmp_gt_u32_e32 vcc, 64, v0
	s_waitcnt vmcnt(4)
	s_and_saveexec_b64 s[6:7], vcc
	ds_write2st64_b32 v42, v40, v41 offset0:70 offset1:71
	s_or_b64 exec, exec, s[6:7]
	s_waitcnt vmcnt(3)
	ds_write_b128 v24, v[8:11]
	s_waitcnt vmcnt(2)
	ds_write_b128 v25, v[12:15]
	s_waitcnt vmcnt(1)
	ds_write_b128 v26, v[16:19]
	s_load_dwordx2 s[10:11], s[0:1], 0x40
	s_movk_i32 s0, 0x84
	v_cmp_gt_u32_e32 vcc, s0, v0
	s_waitcnt vmcnt(0)
	s_and_saveexec_b64 s[0:1], vcc
	ds_write_b128 v27, v[20:23]

amdhsa.kernels:
  - .agpr_count:     0
    .args:
      - .actual_access:  read_only
        .address_space:  global
        .offset:         0
        .size:           8
        .value_kind:     global_buffer
      - .actual_access:  read_only
        .address_space:  global
        .offset:         8
        .size:           8
        .value_kind:     global_buffer
      - .actual_access:  write_only
        .address_space:  global
        .offset:         16
        .size:           8
        .value_kind:     global_buffer
      - .actual_access:  write_only
        .address_space:  global
        .offset:         24
        .size:           8
        .value_kind:     global_buffer
      - .actual_access:  write_only
        .address_space:  global
        .offset:         32
        .size:           8
        .value_kind:     global_buffer
      - .actual_access:  write_only
        .address_space:  global
        .offset:         40
        .size:           8
        .value_kind:     global_buffer
      - .actual_access:  write_only
        .address_space:  global
        .offset:         48
        .size:           8
        .value_kind:     global_buffer
      - .actual_access:  write_only
        .address_space:  global
        .offset:         56
        .size:           8
        .value_kind:     global_buffer
      - .actual_access:  write_only
        .address_space:  global
        .offset:         64
        .size:           8
        .value_kind:     global_buffer
    .group_segment_fixed_size: 18944
    .kernarg_segment_align: 8
    .kernarg_segment_size: 72
    .language:       OpenCL C
    .language_version:
      - 2
      - 0
    .max_flat_workgroup_size: 256
    .name:           _Z6k_prepPKfS0_PfS1_PdS2_PtS3_S3_
    .private_segment_fixed_size: 0
    .sgpr_count:     38
    .sgpr_spill_count: 0
    .symbol:         _Z6k_prepPKfS0_PfS1_PdS2_PtS3_S3_.kd
    .uniform_work_group_size: 1
    .uses_dynamic_stack: false
    .vgpr_count:     29
    .vgpr_spill_count: 0
    .wavefront_size: 64
  - .agpr_count:     16
    .args:
      - .actual_access:  read_only
        .address_space:  global
        .offset:         0
        .size:           8
        .value_kind:     global_buffer
      - .actual_access:  read_only
        .address_space:  global
        .offset:         8
        .size:           8
        .value_kind:     global_buffer
      - .actual_access:  read_only
        .address_space:  global
        .offset:         16
        .size:           8
        .value_kind:     global_buffer
      - .actual_access:  read_only
        .address_space:  global
        .offset:         24
        .size:           8
        .value_kind:     global_buffer
      - .actual_access:  write_only
        .address_space:  global
        .offset:         32
        .size:           8
        .value_kind:     global_buffer
    .group_segment_fixed_size: 256
    .kernarg_segment_align: 8
    .kernarg_segment_size: 40
    .language:       OpenCL C
    .language_version:
      - 2
      - 0
    .max_flat_workgroup_size: 256
    .name:           _Z9k_coarse2PKtS0_PKdS2_Pf
    .private_segment_fixed_size: 0
    .sgpr_count:     46
    .sgpr_spill_count: 0
    .symbol:         _Z9k_coarse2PKtS0_PKdS2_Pf.kd
    .uniform_work_group_size: 1
    .uses_dynamic_stack: false
    .vgpr_count:     224
    .vgpr_spill_count: 0
    .wavefront_size: 64
  - .agpr_count:     0
    .args:
      - .actual_access:  read_only
        .address_space:  global
        .offset:         0
        .size:           8
        .value_kind:     global_buffer
      - .actual_access:  read_only
        .address_space:  global
        .offset:         8
        .size:           8
        .value_kind:     global_buffer
      - .actual_access:  read_only
        .address_space:  global
        .offset:         16
        .size:           8
        .value_kind:     global_buffer
      - .actual_access:  read_only
        .address_space:  global
        .offset:         24
        .size:           8
        .value_kind:     global_buffer
      - .actual_access:  read_only
        .address_space:  global
        .offset:         32
        .size:           8
        .value_kind:     global_buffer
      - .actual_access:  read_only
        .address_space:  global
        .offset:         40
        .size:           8
        .value_kind:     global_buffer
      - .actual_access:  read_only
        .address_space:  global
        .offset:         48
        .size:           8
        .value_kind:     global_buffer
      - .actual_access:  write_only
        .address_space:  global
        .offset:         56
        .size:           8
        .value_kind:     global_buffer
      - .actual_access:  write_only
        .address_space:  global
        .offset:         64
        .size:           8
        .value_kind:     global_buffer
      - .actual_access:  write_only
        .address_space:  global
        .offset:         72
        .size:           8
        .value_kind:     global_buffer
      - .actual_access:  read_only
        .address_space:  global
        .offset:         80
        .size:           8
        .value_kind:     global_buffer
      - .actual_access:  read_only
        .address_space:  global
        .offset:         88
        .size:           8
        .value_kind:     global_buffer
      - .actual_access:  write_only
        .address_space:  global
        .offset:         96
        .size:           8
        .value_kind:     global_buffer
      - .actual_access:  write_only
        .address_space:  global
        .offset:         104
        .size:           8
        .value_kind:     global_buffer
    .group_segment_fixed_size: 30768
    .kernarg_segment_align: 8
    .kernarg_segment_size: 112
    .language:       OpenCL C
    .language_version:
      - 2
      - 0
    .max_flat_workgroup_size: 512
    .name:           _Z7k_fine3PKfS0_PKtS2_PKdS4_S0_PiPfS5_S0_S0_PtS7_
    .private_segment_fixed_size: 0
    .sgpr_count:     106
    .sgpr_spill_count: 4
    .symbol:         _Z7k_fine3PKfS0_PKtS2_PKdS4_S0_PiPfS5_S0_S0_PtS7_.kd
    .uniform_work_group_size: 1
    .uses_dynamic_stack: false
    .vgpr_count:     256
    .vgpr_spill_count: 0
    .wavefront_size: 64
  - .agpr_count:     0
    .args:
      - .actual_access:  read_only
        .address_space:  global
        .offset:         0
        .size:           8
        .value_kind:     global_buffer
      - .actual_access:  read_only
        .address_space:  global
        .offset:         8
        .size:           8
        .value_kind:     global_buffer
      - .actual_access:  read_only
        .address_space:  global
        .offset:         16
        .size:           8
        .value_kind:     global_buffer
      - .actual_access:  read_only
        .address_space:  global
        .offset:         24
        .size:           8
        .value_kind:     global_buffer
      - .actual_access:  read_only
        .address_space:  global
        .offset:         32
        .size:           8
        .value_kind:     global_buffer
      - .actual_access:  read_only
        .address_space:  global
        .offset:         40
        .size:           8
        .value_kind:     global_buffer
      - .actual_access:  write_only
        .address_space:  global
        .offset:         48
        .size:           8
        .value_kind:     global_buffer
      - .actual_access:  write_only
        .address_space:  global
        .offset:         56
        .size:           8
        .value_kind:     global_buffer
      - .actual_access:  write_only
        .address_space:  global
        .offset:         64
        .size:           8
        .value_kind:     global_buffer
    .group_segment_fixed_size: 18512
    .kernarg_segment_align: 8
    .kernarg_segment_size: 72
    .language:       OpenCL C
    .language_version:
      - 2
      - 0
    .max_flat_workgroup_size: 256
    .name:           _Z10k_transferPKtS0_PKfPKiS2_S4_PfS5_S5_
    .private_segment_fixed_size: 0
    .sgpr_count:     46
    .sgpr_spill_count: 0
    .symbol:         _Z10k_transferPKtS0_PKfPKiS2_S4_PfS5_S5_.kd
    .uniform_work_group_size: 1
    .uses_dynamic_stack: false
    .vgpr_count:     49
    .vgpr_spill_count: 0
    .wavefront_size: 64
